# P10 small trims: token-prologue max reduction as 4 v_max_f32_dpp (was mov 0 / mov_dpp / canonicalise / max), remaining canonicalise copies, dead index-vector copies, one counted wait before the set-A
# speedup vs baseline: 1.0239x; 1.0046x over previous
; __device__ __forceinline__ void expert_tokens(const unsigned char* __restrict__ UV, const float* __restrict__ US, const float* __restrict__ VS, ...
;     ...
;         float sy = 0.f;
;         const float sumc = wave_sum(sumc_l) * (0.25f / 4096.f);
; #pragma unroll
;         for (int i = 0; i < 16; ++i) { acc[i] = acc[i] * 4096.f - 7.5f * sumc; sy += acc[i] * acc[i]; }
;         const float ry = rsqrtf(wave_sum(sy) * (1.f / 1024.f) + EPS);
.LBB0_1013:
	v_add_f32_dpp v66, v252, v252 quad_perm:[1,0,3,2] row_mask:0xf bank_mask:0xf bound_ctrl:1
	s_ashr_i32 s21, s20, 31
	s_lshl_b64 s[4:5], s[20:21], 12
	v_add_f32_dpp v66, v66, v66 quad_perm:[2,3,0,1] row_mask:0xf bank_mask:0xf bound_ctrl:1
	v_lshl_add_u64 v[162:163], v[200:201], 0, s[4:5]
	s_waitcnt vmcnt(31)
	v_mov_b64_e32 v[190:191], v[80:81]
	v_add_f32_dpp v66, v66, v66 row_ror:4 row_mask:0xf bank_mask:0xf bound_ctrl:1
	s_waitcnt vmcnt(30)
	v_mov_b64_e32 v[186:187], v[76:77]
	s_waitcnt vmcnt(29)
	v_mov_b64_e32 v[182:183], v[88:89]
	v_add_f32_dpp v66, v66, v66 row_ror:8 row_mask:0xf bank_mask:0xf bound_ctrl:1
	v_mov_b32_e32 v67, v66
	s_nop 1
	v_permlane16_swap_b32_e32 v66, v67
	v_add_f32_e32 v66, v66, v67
	v_mov_b32_e32 v67, v66
	s_nop 1
	v_permlane32_swap_b32_e32 v66, v67
	v_add_f32_e32 v66, v66, v67
	v_mul_f32_e32 v66, 0x38800000, v66
	v_mul_f32_e32 v66, 0x40f00000, v66
	v_pk_add_f32 v[224:225], v[224:225], v[220:221] neg_lo:[0,1] neg_hi:[0,1]
	v_pk_add_f32 v[222:223], v[222:223], v[218:219] neg_lo:[0,1] neg_hi:[0,1]
	v_pk_add_f32 v[216:217], v[216:217], v[212:213] neg_lo:[0,1] neg_hi:[0,1]
	v_pk_add_f32 v[214:215], v[214:215], v[210:211] neg_lo:[0,1] neg_hi:[0,1]
	s_mov_b32 s62, 0x43800000
	v_pk_fma_f32 v[118:119], v[224:225], s[16:17], v[66:67] op_sel_hi:[1,0,0] neg_lo:[0,0,1] neg_hi:[0,0,1]
	v_pk_fma_f32 v[144:145], v[222:223], s[16:17], v[66:67] op_sel_hi:[1,0,0] neg_lo:[0,0,1] neg_hi:[0,0,1]
	v_pk_mul_f32 v[68:69], v[118:119], v[118:119]
	v_pk_mul_f32 v[70:71], v[144:145], v[144:145]
	v_add_f32_e32 v68, v68, v69
	v_pk_fma_f32 v[148:149], v[220:221], s[62:63], v[66:67] op_sel_hi:[1,0,0] neg_lo:[0,0,1] neg_hi:[0,0,1]
	v_add_f32_e32 v68, v70, v68
	v_pk_mul_f32 v[72:73], v[148:149], v[148:149]
	v_add_f32_e32 v68, v71, v68
	v_pk_fma_f32 v[150:151], v[218:219], s[62:63], v[66:67] op_sel_hi:[1,0,0] neg_lo:[0,0,1] neg_hi:[0,0,1]
	v_add_f32_e32 v68, v72, v68
	v_pk_mul_f32 v[114:115], v[150:151], v[150:151]
	v_add_f32_e32 v68, v73, v68
	v_pk_fma_f32 v[152:153], v[216:217], s[16:17], v[66:67] op_sel_hi:[1,0,0] neg_lo:[0,0,1] neg_hi:[0,0,1]
	v_add_f32_e32 v68, v114, v68
	v_pk_mul_f32 v[116:117], v[152:153], v[152:153]
	v_add_f32_e32 v68, v115, v68
	v_pk_fma_f32 v[154:155], v[214:215], s[16:17], v[66:67] op_sel_hi:[1,0,0] neg_lo:[0,0,1] neg_hi:[0,0,1]
	v_add_f32_e32 v68, v116, v68
	v_pk_mul_f32 v[146:147], v[154:155], v[154:155]
	v_add_f32_e32 v68, v117, v68
	v_pk_fma_f32 v[156:157], v[212:213], s[62:63], v[66:67] op_sel_hi:[1,0,0] neg_lo:[0,0,1] neg_hi:[0,0,1]
	v_add_f32_e32 v68, v146, v68
	v_pk_mul_f32 v[158:159], v[156:157], v[156:157]
	v_add_f32_e32 v68, v147, v68
	v_pk_fma_f32 v[160:161], v[210:211], s[62:63], v[66:67] op_sel_hi:[1,0,0] neg_lo:[0,0,1] neg_hi:[0,0,1]
	v_add_f32_e32 v68, v158, v68
	v_pk_mul_f32 v[66:67], v[160:161], v[160:161]
	v_add_f32_e32 v68, v159, v68
	v_add_f32_e32 v66, v66, v68
	v_add_f32_e32 v66, v67, v66
	ds_read_b128 v[114:117], v240 offset:8192
	ds_read2st64_b64 v[70:73], v239 offset0:34 offset1:35
	v_add_f32_dpp v66, v66, v66 quad_perm:[1,0,3,2] row_mask:0xf bank_mask:0xf bound_ctrl:1
	s_waitcnt vmcnt(28)
	v_mov_b64_e32 v[178:179], v[84:85]
	s_waitcnt vmcnt(27)
	v_mov_b64_e32 v[174:175], v[96:97]
	v_add_f32_dpp v66, v66, v66 quad_perm:[2,3,0,1] row_mask:0xf bank_mask:0xf bound_ctrl:1
	s_waitcnt vmcnt(26)
; #define LAS __attribute__((address_space(3)))
; __device__ __forceinline__ void expert_tokens(const unsigned char* __restrict__ UV, const float* __restrict__ US, const float* __restrict__ VS, ...
;     ...
;         const float ry = rsqrtf(wave_sum(sy) * (1.f / 1024.f) + EPS);
;         const float pscale = (t < 2048) ? 1.f + pd : 1.f;
; #pragma unroll
;         for (int j = 0; j < 4; ++j) { const f32x4 y = (f32x4){acc[4 * j], acc[4 * j + 1], acc[4 * j + 2], acc[4 * j + 3]};
;             float* op = out + (size_t)t * 1024 + 256 * j + 4 * lane;
;             const u32x2 xw = *(const LAS u32x2*)(xrow + 512 * j + 8 * lane);
;             { const f32x4 ov_ = pscale * (f32x4){__uint_as_float(xw.x << 16), __uint_as_float(xw.x & 0xffff0000u), __uint_as_float(xw.y << 16), __uint_as_float(xw.y & 0xffff0000u)} + pscale * *(const LAS f32x4*)(pvt + 2048 + 256 * j + 4 * lane) * (y * ry); __builtin_nontemporal_store(ov_, (f32x4*)op); } }
;         ci0 = ni0; ci1 = ni1; cg0 = ng0; cg1 = ng1; csu0 = nsu0; csu1 = nsu1; csv0 = nsv0; csv1 = nsv1;
	v_mov_b64_e32 v[170:171], v[92:93]
	v_mov_b64_e32 v[188:189], v[78:79]
	v_add_f32_dpp v66, v66, v66 row_ror:4 row_mask:0xf bank_mask:0xf bound_ctrl:1
	v_mov_b64_e32 v[184:185], v[74:75]
	v_mov_b64_e32 v[180:181], v[86:87]
	v_add_f32_dpp v66, v66, v66 row_ror:8 row_mask:0xf bank_mask:0xf bound_ctrl:1
	v_mov_b32_e32 v67, v66
	s_nop 1
	v_permlane16_swap_b32_e32 v66, v67
	v_add_f32_e32 v66, v66, v67
	v_mov_b32_e32 v67, v66
	s_nop 1
	v_permlane32_swap_b32_e32 v66, v67
	v_add_f32_e32 v66, v66, v67
	v_fmamk_f32 v66, v66, 0x3a800000, v226
	v_mul_f32_e32 v67, 0x4b800000, v66
	v_cmp_gt_f32_e32 vcc, s9, v66
	v_mov_b64_e32 v[176:177], v[82:83]
	v_mov_b64_e32 v[172:173], v[94:95]
	v_cndmask_b32_e32 v66, v66, v67, vcc
	v_rsq_f32_e32 v66, v66
	v_mov_b64_e32 v[168:169], v[90:91]
	s_mov_b64 s[92:93], s[86:87]
	s_mov_b64 s[86:87], s[88:89]
	s_mov_b64 s[88:89], s[92:93]
	v_mul_f32_e32 v67, 0x45800000, v66
	v_cndmask_b32_e32 v158, v66, v67, vcc
	ds_read2st64_b64 v[66:69], v239 offset0:32 offset1:33
	v_pk_mul_f32 v[166:167], v[144:145], v[158:159] op_sel_hi:[1,0]
	ds_read_b128 v[144:147], v240 offset:9216
	v_pk_mul_f32 v[118:119], v[118:119], v[158:159] op_sel_hi:[1,0]
	s_and_b64 vcc, exec, s[18:19]
	s_waitcnt lgkmcnt(1)
	v_lshlrev_b32_e32 v164, 16, v66
	v_and_b32_e32 v165, 0xffff0000, v66
	v_lshlrev_b32_e32 v66, 16, v67
	v_and_b32_e32 v67, 0xffff0000, v67
	v_pk_fma_f32 v[116:117], v[116:117], v[166:167], v[66:67]
	v_pk_fma_f32 v[114:115], v[114:115], v[118:119], v[164:165]
	global_store_dwordx4 v[162:163], v[114:117], off nt
	v_lshlrev_b32_e32 v66, 16, v68
	v_and_b32_e32 v67, 0xffff0000, v68
	v_lshlrev_b32_e32 v68, 16, v69
	v_and_b32_e32 v69, 0xffff0000, v69
	v_pk_mul_f32 v[114:115], v[148:149], v[158:159] op_sel_hi:[1,0]
	v_pk_mul_f32 v[116:117], v[150:151], v[158:159] op_sel_hi:[1,0]
	s_waitcnt lgkmcnt(0)
	v_pk_fma_f32 v[66:67], v[144:145], v[114:115], v[66:67]
	v_pk_fma_f32 v[68:69], v[146:147], v[116:117], v[68:69]
	global_store_dwordx4 v[162:163], v[66:69], off offset:1024 nt
	ds_read_b128 v[66:69], v240 offset:10240
	ds_read_b128 v[114:117], v240 offset:11264
	v_lshlrev_b32_e32 v118, 16, v70
	v_and_b32_e32 v119, 0xffff0000, v70
	v_lshlrev_b32_e32 v70, 16, v71
	v_and_b32_e32 v71, 0xffff0000, v71
	v_pk_mul_f32 v[144:145], v[152:153], v[158:159] op_sel_hi:[1,0]
	v_pk_mul_f32 v[146:147], v[154:155], v[158:159] op_sel_hi:[1,0]
	s_waitcnt lgkmcnt(1)
	v_pk_fma_f32 v[66:67], v[66:67], v[144:145], v[118:119]
	v_pk_fma_f32 v[68:69], v[68:69], v[146:147], v[70:71]
	global_store_dwordx4 v[162:163], v[66:69], off offset:2048 nt
	v_pk_mul_f32 v[70:71], v[156:157], v[158:159] op_sel_hi:[1,0]
	s_waitcnt vmcnt(28)
	v_mov_b64_e32 v[166:167], v[104:105]
	v_lshlrev_b32_e32 v66, 16, v72
	v_and_b32_e32 v67, 0xffff0000, v72
	v_lshlrev_b32_e32 v68, 16, v73
	v_and_b32_e32 v69, 0xffff0000, v73
	v_pk_mul_f32 v[72:73], v[160:161], v[158:159] op_sel_hi:[1,0]
	s_waitcnt lgkmcnt(0)
	v_pk_fma_f32 v[66:67], v[114:115], v[70:71], v[66:67]
	v_pk_fma_f32 v[68:69], v[116:117], v[72:73], v[68:69]
	s_waitcnt vmcnt(26)
	v_mov_b64_e32 v[158:159], v[112:113]
	global_store_dwordx4 v[162:163], v[66:69], off offset:3072 nt
	v_mov_b64_e32 v[162:163], v[100:101]
	v_mov_b64_e32 v[156:157], v[110:111]
	s_waitcnt vmcnt(26)
	v_mov_b64_e32 v[154:155], v[108:109]
	s_waitcnt vmcnt(25)
	v_mov_b64_e32 v[150:151], v[126:127]
	s_waitcnt vmcnt(24)
	v_mov_b64_e32 v[146:147], v[122:123]
	s_waitcnt vmcnt(23)
	v_mov_b64_e32 v[116:117], v[132:133]
	s_waitcnt vmcnt(22)
	v_mov_b64_e32 v[112:113], v[128:129]
	s_waitcnt vmcnt(21)
	v_mov_b64_e32 v[70:71], v[140:141]
	s_waitcnt vmcnt(20)
	v_mov_b64_e32 v[66:67], v[136:137]
	v_mov_b64_e32 v[164:165], v[102:103]
	v_mov_b64_e32 v[160:161], v[98:99]
	v_mov_b64_e32 v[152:153], v[106:107]
	v_mov_b64_e32 v[148:149], v[124:125]
	v_mov_b64_e32 v[144:145], v[120:121]
	v_mov_b64_e32 v[118:119], v[134:135]
	v_mov_b64_e32 v[114:115], v[130:131]
	v_mov_b64_e32 v[72:73], v[142:143]
	v_mov_b64_e32 v[68:69], v[138:139]
	v_mov_b32_e32 v229, v237
	v_mov_b32_e32 v230, v238
	v_mov_b32_e32 v233, v241
	v_mov_b32_e32 v234, v0
	v_mov_b32_e32 v235, v245
	v_mov_b32_e32 v236, v246
	s_mov_b32 s20, s34
	s_cbranch_vccnz .LBB0_1025

; #define LAS __attribute__((address_space(3)))
; __device__ __forceinline__ void expert_tokens(const unsigned char* __restrict__ UV, const float* __restrict__ US, const float* __restrict__ VS, ...
;     ...
;         const LAS unsigned char* xrow = xslot + (t & 1) * 2048;
;         float nsu0 = 0.f, nsu1 = 0.f, nsv0 = 0.f, nsv1 = 0.f;
;         float hv[16]; float mx = 0.f;
;         { float s2 = 0.f; f32x4 x1[4];
; #pragma unroll
;           for (int j = 0; j < 4; ++j) { const u32x2 xw = *(const LAS u32x2*)(xrow + 512 * j + 8 * lane);
;               x1[j] = (f32x4){__uint_as_float(xw.x << 16), __uint_as_float(xw.x & 0xffff0000u), __uint_as_float(xw.y << 16), __uint_as_float(xw.y & 0xffff0000u)}; s2 += x1[j].x * x1[j].x + x1[j].y * x1[j].y + x1[j].z * x1[j].z + x1[j].w * x1[j].w; }
;           const float r2 = rsqrtf(wave_sum(s2) * (1.f / 1024.f) + EPS);
; #pragma unroll
;           for (int j = 0; j < 4; ++j) { const f32x4 h = x1[j] * r2 * *(const LAS f32x4*)(pvt + 256 * j + 4 * lane) + *(const LAS f32x4*)(pvt + 1024 + 256 * j + 4 * lane);
;               hv[4 * j] = h.x; hv[4 * j + 1] = h.y; hv[4 * j + 2] = h.z; hv[4 * j + 3] = h.w;
;               mx = fmaxf(mx, fmaxf(fmaxf(fabsf(h.x), fabsf(h.y)), fmaxf(fabsf(h.z), fabsf(h.w)))); } }
;         mx = wave_max(mx);
;         const float sx = mx > 0.f ? mx / 119.f : 1.f, isx = 1.f / sx;
.LBB0_1018:
	s_lshl_b32 s4, s20, 11
	s_and_b32 s4, s4, 0x800
	v_add_u32_e32 v239, s4, v195
	ds_read2st64_b64 v[74:77], v239 offset0:32 offset1:33
	ds_read2st64_b64 v[78:81], v239 offset0:34 offset1:35
	v_lshl_add_u32 v240, v192, 2, v0
	s_waitcnt lgkmcnt(0)
	v_and_b32_e32 v83, 0xffff0000, v74
	v_and_b32_e32 v91, 0xffff0000, v76
	v_lshlrev_b32_e32 v82, 16, v74
	v_lshlrev_b32_e32 v84, 16, v75
	v_and_b32_e32 v85, 0xffff0000, v75
	v_mul_f32_e32 v74, v83, v83
	v_lshlrev_b32_e32 v90, 16, v76
	v_mul_f32_e32 v75, v91, v91
	v_fmac_f32_e32 v74, v82, v82
	v_lshlrev_b32_e32 v92, 16, v77
	v_fmac_f32_e32 v75, v90, v90
	v_fmac_f32_e32 v74, v84, v84
	v_and_b32_e32 v93, 0xffff0000, v77
	v_fmac_f32_e32 v75, v92, v92
	v_fmac_f32_e32 v74, v85, v85
	v_fmac_f32_e32 v75, v93, v93
	v_and_b32_e32 v95, 0xffff0000, v78
	v_add_f32_e32 v74, v74, v75
	v_lshlrev_b32_e32 v94, 16, v78
	v_mul_f32_e32 v75, v95, v95
	v_lshlrev_b32_e32 v96, 16, v79
	v_fmac_f32_e32 v75, v94, v94
	v_and_b32_e32 v97, 0xffff0000, v79
	v_fmac_f32_e32 v75, v96, v96
	v_fmac_f32_e32 v75, v97, v97
	v_and_b32_e32 v99, 0xffff0000, v80
	v_add_f32_e32 v74, v74, v75
	v_lshlrev_b32_e32 v98, 16, v80
	v_mul_f32_e32 v75, v99, v99
	v_lshlrev_b32_e32 v100, 16, v81
	v_fmac_f32_e32 v75, v98, v98
	v_and_b32_e32 v101, 0xffff0000, v81
	v_fmac_f32_e32 v75, v100, v100
	v_fmac_f32_e32 v75, v101, v101
	v_add_f32_e32 v74, v74, v75
	v_mov_b32_e32 v241, 0
	s_mov_b32 s21, 32
	v_add_f32_dpp v74, v74, v74 quad_perm:[1,0,3,2] row_mask:0xf bank_mask:0xf bound_ctrl:1
	s_mov_b32 s25, 0
	v_mov_b32_e32 v245, 0
	v_add_f32_dpp v74, v74, v74 quad_perm:[2,3,0,1] row_mask:0xf bank_mask:0xf bound_ctrl:1
	v_mov_b32_e32 v246, 0
	v_mov_b32_e32 v252, 0
	v_add_f32_dpp v74, v74, v74 row_ror:4 row_mask:0xf bank_mask:0xf bound_ctrl:1
	v_mov_b32_e32 v224, 0
	v_mov_b32_e32 v225, 0
	v_add_f32_dpp v74, v74, v74 row_ror:8 row_mask:0xf bank_mask:0xf bound_ctrl:1
	v_mov_b32_e32 v75, v74
	s_nop 1
	v_permlane16_swap_b32_e32 v74, v75
	v_add_f32_e32 v74, v74, v75
	v_mov_b32_e32 v75, v74
	s_nop 1
	v_permlane32_swap_b32_e32 v74, v75
	v_add_f32_e32 v74, v74, v75
	v_fmamk_f32 v74, v74, 0x3a800000, v226
	v_mul_f32_e32 v75, 0x4b800000, v74
	v_cmp_gt_f32_e32 vcc, s9, v74
	v_mov_b32_e32 v222, 0
	v_mov_b32_e32 v223, 0
	v_cndmask_b32_e32 v74, v74, v75, vcc
	v_rsq_f32_e32 v74, v74
	v_mov_b32_e32 v220, 0
	v_mov_b32_e32 v221, 0
	v_mov_b32_e32 v218, 0
	v_mul_f32_e32 v75, 0x45800000, v74
	v_cndmask_b32_e32 v102, v74, v75, vcc
	ds_read_b128 v[74:77], v240
	ds_read_b128 v[78:81], v240 offset:4096
	v_pk_mul_f32 v[104:105], v[82:83], v[102:103] op_sel_hi:[1,0]
	v_pk_mul_f32 v[106:107], v[84:85], v[102:103] op_sel_hi:[1,0]
	ds_read_b128 v[82:85], v240 offset:1024
	ds_read_b128 v[86:89], v240 offset:5120
	v_pk_mul_f32 v[96:97], v[96:97], v[102:103] op_sel_hi:[1,0]
	s_waitcnt lgkmcnt(2)
	v_pk_fma_f32 v[106:107], v[76:77], v[106:107], v[80:81]
	v_pk_mul_f32 v[76:77], v[92:93], v[102:103] op_sel_hi:[1,0]
	v_pk_fma_f32 v[104:105], v[74:75], v[104:105], v[78:79]
	v_pk_mul_f32 v[74:75], v[90:91], v[102:103] op_sel_hi:[1,0]
	s_waitcnt lgkmcnt(0)
	v_pk_fma_f32 v[90:91], v[84:85], v[76:77], v[88:89]
	v_max_f32_e64 v0, |v106|, |v107|
	v_pk_fma_f32 v[92:93], v[82:83], v[74:75], v[86:87]
	v_max_f32_e64 v74, |v90|, |v91|
	v_max3_f32 v0, |v104|, |v105|, v0
	v_max3_f32 v74, |v92|, |v93|, v74
	v_max3_f32 v0, v0, 0, v74
	ds_read_b128 v[74:77], v240 offset:2048
	ds_read_b128 v[78:81], v240 offset:6144
	ds_read_b128 v[82:85], v240 offset:3072
	ds_read_b128 v[86:89], v240 offset:7168
	v_pk_mul_f32 v[94:95], v[94:95], v[102:103] op_sel_hi:[1,0]
	v_mov_b32_e32 v219, 0
	v_mov_b32_e32 v216, 0
	s_waitcnt lgkmcnt(2)
	v_pk_fma_f32 v[76:77], v[76:77], v[96:97], v[80:81]
	v_pk_fma_f32 v[74:75], v[74:75], v[94:95], v[78:79]
	v_max_f32_e64 v78, |v76|, |v77|
	v_pk_mul_f32 v[80:81], v[100:101], v[102:103] op_sel_hi:[1,0]
	v_max3_f32 v94, |v74|, |v75|, v78
	v_pk_mul_f32 v[78:79], v[98:99], v[102:103] op_sel_hi:[1,0]
	s_waitcnt lgkmcnt(0)
	v_pk_fma_f32 v[80:81], v[84:85], v[80:81], v[88:89]
	v_pk_fma_f32 v[78:79], v[82:83], v[78:79], v[86:87]
	v_max_f32_e64 v82, |v80|, |v81|
	v_max3_f32 v82, |v78|, |v79|, v82
	v_max3_f32 v0, v0, v94, v82
	v_mov_b32_e32 v217, 0
	v_mov_b32_e32 v214, 0
	v_max_f32_dpp v0, v0, v0 quad_perm:[1,0,3,2] row_mask:0xf bank_mask:0xf
	v_mov_b32_e32 v215, 0
	v_mov_b32_e32 v212, 0
	v_max_f32_dpp v0, v0, v0 quad_perm:[2,3,0,1] row_mask:0xf bank_mask:0xf
	v_mov_b32_e32 v213, 0
	v_mov_b32_e32 v210, 0
	v_max_f32_dpp v0, v0, v0 row_ror:4 row_mask:0xf bank_mask:0xf
	v_mov_b32_e32 v211, 0
	s_nop 0
	v_max_f32_dpp v0, v0, v0 row_ror:8 row_mask:0xf bank_mask:0xf
	v_mov_b32_e32 v82, v0
	s_nop 1
	v_permlane16_swap_b32_e32 v0, v82
	v_max_f32_e32 v0, v0, v82
	v_mov_b32_e32 v82, v0
	s_nop 1
	v_permlane32_swap_b32_e32 v0, v82
	v_max_f32_e32 v0, v0, v82
	v_div_scale_f32 v82, s[4:5], s27, s27, v0
	v_rcp_f32_e32 v83, v82
	s_nop 0
	v_fma_f32 v84, -v82, v83, 1.0
	v_fmac_f32_e32 v83, v84, v83
	v_div_scale_f32 v84, vcc, v0, s27, v0
	v_mul_f32_e32 v85, v84, v83
	v_fma_f32 v86, -v82, v85, v84
	v_fmac_f32_e32 v85, v86, v83
	v_fma_f32 v82, -v82, v85, v84
	v_div_fmas_f32 v82, v82, v83, v85
	v_div_fixup_f32 v82, v82, s27, v0
	v_cmp_lt_f32_e32 vcc, 0, v0
	s_nop 1
	v_cndmask_b32_e32 v244, 1.0, v82, vcc
	v_div_scale_f32 v0, s[4:5], v244, v244, 1.0
	v_rcp_f32_e32 v82, v0
	s_nop 0
	v_fma_f32 v83, -v0, v82, 1.0
	v_fmac_f32_e32 v82, v83, v82
	v_div_scale_f32 v83, vcc, 1.0, v244, 1.0
	v_mul_f32_e32 v84, v83, v82
	v_fma_f32 v85, -v0, v84, v83
	v_fmac_f32_e32 v84, v85, v82
	v_fma_f32 v0, -v0, v84, v83
	v_div_fmas_f32 v0, v0, v82, v84
	v_div_fixup_f32 v0, v0, v244, 1.0
	v_mul_f32_e32 v82, v104, v0
	v_mul_f32_e32 v83, v92, v0
; __device__ __forceinline__ void expert_tokens(const unsigned char* __restrict__ UV, const float* __restrict__ US, const float* __restrict__ VS, ...
;     ...
;         const float sx = mx > 0.f ? mx / 119.f : 1.f, isx = 1.f / sx;
;         int xh[2], xl[2]; int xs = 0;
; #pragma unroll
;         for (int m = 0; m < 2; ++m) { unsigned wh = 0, wl = 0;
; #pragma unroll
;             for (int k = 0; k < 8; ++k) { const int pos = 8 * m + (k >> 1) + 4 * (k & 1); const int q = (int)rintf(hv[pos] * isx); xs += q;
;                 const int ql = ((q + 8) & 15) - 8, qh = (q - ql) >> 4;
;                 wl |= (unsigned)(ql & 15) << (4 * k); wh |= (unsigned)(qh & 15) << (4 * k); }
;             xh[m] = (int)wh; xl[m] = (int)wl; }
; #pragma unroll
;         for (int o = 1; o < 64; o <<= 1) xs += __shfl_xor(xs, o);
;         const float xoff = 0.5f * (float)xs;
	v_rndne_f32_e32 v82, v82
	v_rndne_f32_e32 v83, v83
	v_cvt_i32_f32_e32 v82, v82
	v_cvt_i32_f32_e32 v83, v83
	v_mul_f32_e32 v87, v105, v0
	v_rndne_f32_e32 v87, v87
	v_mul_f32_e32 v89, v93, v0
	v_cvt_i32_f32_e32 v87, v87
	v_rndne_f32_e32 v89, v89
	v_bfe_i32 v84, v82, 0, 4
	v_bfe_i32 v86, v83, 0, 4
	v_cvt_i32_f32_e32 v89, v89
	v_sub_u32_e32 v84, v82, v84
	v_sub_u32_e32 v86, v83, v86
	v_lshrrev_b32_e32 v84, 4, v84
	v_and_b32_e32 v86, 0xf0, v86
	v_mul_f32_e32 v92, v106, v0
	v_add_u32_e32 v85, v82, v83
	v_and_or_b32 v84, v84, 15, v86
	v_bfe_i32 v86, v87, 0, 4
	v_rndne_f32_e32 v92, v92
	v_mul_f32_e32 v90, v90, v0
	v_sub_u32_e32 v86, v87, v86
	v_lshlrev_b32_e32 v88, 8, v87
	v_add3_u32 v85, v85, v87, v89
	v_bfe_i32 v87, v89, 0, 4
	v_cvt_i32_f32_e32 v92, v92
	v_rndne_f32_e32 v90, v90
	v_sub_u32_e32 v87, v89, v87
	v_cvt_i32_f32_e32 v90, v90
	v_lshlrev_b32_e32 v86, 4, v86
	v_lshlrev_b32_e32 v87, 8, v87
	v_mul_f32_e32 v93, v107, v0
	v_and_b32_e32 v86, 0xf00, v86
	v_and_b32_e32 v87, 0xf000, v87
	v_rndne_f32_e32 v93, v93
	v_mul_f32_e32 v91, v91, v0
	v_or3_b32 v84, v84, v86, v87
	v_bfe_i32 v86, v92, 0, 4
	v_cvt_i32_f32_e32 v93, v93
	v_rndne_f32_e32 v91, v91
	v_sub_u32_e32 v86, v92, v86
	v_lshlrev_b32_e32 v87, 16, v92
	v_add3_u32 v85, v85, v92, v90
	v_bfe_i32 v92, v90, 0, 4
	v_cvt_i32_f32_e32 v91, v91
	v_lshlrev_b32_e32 v83, 4, v83
	v_lshlrev_b32_e32 v86, 12, v86
	v_sub_u32_sdwa v92, v90, v92 dst_sel:WORD_1 dst_unused:UNUSED_PAD src0_sel:DWORD src1_sel:DWORD
	v_mul_f32_e32 v74, v74, v0
	v_mul_f32_e32 v78, v78, v0
	v_and_b32_e32 v83, 0xf0, v83
	v_lshlrev_b32_e32 v89, 12, v89
	v_and_b32_e32 v86, 0xf0000, v86
	v_and_b32_e32 v92, 0xf00000, v92
	v_rndne_f32_e32 v74, v74
	v_rndne_f32_e32 v78, v78
	v_and_b32_e32 v88, 0xf00, v88
	v_and_b32_e32 v89, 0xf000, v89
	v_lshlrev_b32_e32 v90, 20, v90
	v_or3_b32 v84, v84, v86, v92
	v_bfe_i32 v86, v93, 0, 4
	v_and_or_b32 v82, v82, 15, v83
	v_cvt_i32_f32_e32 v74, v74
	v_cvt_i32_f32_e32 v78, v78
	v_and_b32_e32 v87, 0xf0000, v87
	v_and_b32_e32 v90, 0xf00000, v90
	v_sub_u32_e32 v86, v93, v86
	v_lshlrev_b32_e32 v92, 24, v93
	v_bfe_i32 v94, v91, 0, 4
	v_or3_b32 v82, v82, v88, v89
	v_mul_f32_e32 v75, v75, v0
	v_and_b32_e32 v92, 0xf000000, v92
	v_lshlrev_b32_e32 v86, 20, v86
	v_add3_u32 v85, v85, v93, v91
	v_lshlrev_b32_e32 v93, 28, v91
	v_sub_u32_sdwa v91, v91, v94 dst_sel:BYTE_3 dst_unused:UNUSED_PAD src0_sel:DWORD src1_sel:DWORD
	v_or3_b32 v82, v82, v87, v90
	v_rndne_f32_e32 v75, v75
	v_mul_f32_e32 v79, v79, v0
	v_and_b32_e32 v86, 0xf000000, v86
	v_or3_b32 v247, v82, v92, v93
	v_and_b32_e32 v82, 0xf0000000, v91
	v_cvt_i32_f32_e32 v75, v75
	v_rndne_f32_e32 v79, v79
	v_or3_b32 v248, v84, v86, v82
	v_bfe_i32 v82, v74, 0, 4
	v_bfe_i32 v84, v78, 0, 4
	v_cvt_i32_f32_e32 v79, v79
	v_sub_u32_e32 v82, v74, v82
	v_sub_u32_e32 v84, v78, v84
	v_lshrrev_b32_e32 v82, 4, v82
	v_and_b32_e32 v84, 0xf0, v84
	v_add3_u32 v83, v85, v74, v78
	v_and_or_b32 v82, v82, 15, v84
	v_bfe_i32 v84, v75, 0, 4
	v_sub_u32_e32 v84, v75, v84
	v_lshlrev_b32_e32 v85, 8, v75
	v_add3_u32 v75, v83, v75, v79
	v_bfe_i32 v83, v79, 0, 4
	v_sub_u32_e32 v83, v79, v83
	v_mul_f32_e32 v76, v76, v0
	v_mul_f32_e32 v80, v80, v0
	v_lshlrev_b32_e32 v84, 4, v84
	v_lshlrev_b32_e32 v83, 8, v83
	v_rndne_f32_e32 v76, v76
	v_rndne_f32_e32 v80, v80
	v_mul_f32_e32 v77, v77, v0
	v_mul_f32_e32 v0, v81, v0
	v_and_b32_e32 v84, 0xf00, v84
	v_and_b32_e32 v83, 0xf000, v83
	v_cvt_i32_f32_e32 v76, v76
	v_cvt_i32_f32_e32 v80, v80
	v_rndne_f32_e32 v77, v77
	v_rndne_f32_e32 v0, v0
	v_cvt_i32_f32_e32 v77, v77
	v_cvt_i32_f32_e32 v0, v0
	v_or3_b32 v81, v82, v84, v83
	v_and_b32_e32 v83, 64, v228
	v_add_u32_e32 v83, 64, v83
	v_xor_b32_e32 v84, 1, v228
	v_cmp_lt_i32_e32 vcc, v84, v83
	v_add3_u32 v75, v75, v76, v80
	v_add3_u32 v75, v75, v77, v0
	v_cndmask_b32_e32 v84, v228, v84, vcc
	v_lshlrev_b32_e32 v84, 2, v84
	ds_bpermute_b32 v84, v84, v75
	v_bfe_i32 v82, v76, 0, 4
	v_sub_u32_e32 v82, v76, v82
	v_bfe_i32 v86, v80, 0, 4
	v_lshlrev_b32_e32 v78, 4, v78
	s_waitcnt lgkmcnt(0)
	v_add_u32_e32 v75, v75, v84
	v_xor_b32_e32 v84, 2, v228
	v_cmp_lt_i32_e32 vcc, v84, v83
	v_lshlrev_b32_e32 v82, 12, v82
	v_sub_u32_sdwa v86, v80, v86 dst_sel:WORD_1 dst_unused:UNUSED_PAD src0_sel:DWORD src1_sel:DWORD
	v_cndmask_b32_e32 v84, v228, v84, vcc
	v_lshlrev_b32_e32 v84, 2, v84
	ds_bpermute_b32 v84, v84, v75
	v_and_b32_e32 v78, 0xf0, v78
	v_lshlrev_b32_e32 v79, 12, v79
	v_and_b32_e32 v82, 0xf0000, v82
	v_and_b32_e32 v86, 0xf00000, v86
	s_waitcnt lgkmcnt(0)
	v_add_u32_e32 v75, v75, v84
	v_xor_b32_e32 v84, 4, v228
	v_cmp_lt_i32_e32 vcc, v84, v83
	v_and_b32_e32 v85, 0xf00, v85
	v_and_b32_e32 v79, 0xf000, v79
	v_cndmask_b32_e32 v84, v228, v84, vcc
	v_lshlrev_b32_e32 v84, 2, v84
	ds_bpermute_b32 v84, v84, v75
	v_lshlrev_b32_e32 v76, 16, v76
	v_lshlrev_b32_e32 v80, 20, v80
	v_or3_b32 v81, v81, v82, v86
	v_bfe_i32 v82, v77, 0, 4
	s_waitcnt lgkmcnt(0)
	v_add_u32_e32 v75, v75, v84
	v_xor_b32_e32 v84, 8, v228
	v_cmp_lt_i32_e32 vcc, v84, v83
	v_and_or_b32 v74, v74, 15, v78
	v_and_b32_e32 v76, 0xf0000, v76
	v_cndmask_b32_e32 v84, v228, v84, vcc
	v_lshlrev_b32_e32 v84, 2, v84
	ds_bpermute_b32 v84, v84, v75
	v_and_b32_e32 v80, 0xf00000, v80
	v_sub_u32_e32 v82, v77, v82
	v_lshlrev_b32_e32 v77, 24, v77
	v_or3_b32 v74, v74, v85, v79
	s_waitcnt lgkmcnt(0)
	v_add_u32_e32 v75, v75, v84
	v_xor_b32_e32 v84, 16, v228
	v_cmp_lt_i32_e32 vcc, v84, v83
	v_and_b32_e32 v77, 0xf000000, v77
	v_lshlrev_b32_e32 v86, 28, v0
	v_cndmask_b32_e32 v84, v228, v84, vcc
	v_lshlrev_b32_e32 v84, 2, v84
	ds_bpermute_b32 v84, v84, v75
	v_or3_b32 v74, v74, v76, v80
	v_or3_b32 v249, v74, v77, v86
	v_bfe_i32 v87, v0, 0, 4
	v_lshlrev_b32_e32 v82, 20, v82
	s_waitcnt lgkmcnt(0)
	v_add_u32_e32 v75, v75, v84
	v_xor_b32_e32 v84, 32, v228
	v_cmp_lt_i32_e32 vcc, v84, v83
	v_sub_u32_sdwa v0, v0, v87 dst_sel:BYTE_3 dst_unused:UNUSED_PAD src0_sel:DWORD src1_sel:DWORD
	v_and_b32_e32 v82, 0xf000000, v82
	v_cndmask_b32_e32 v83, v228, v84, vcc
	v_lshlrev_b32_e32 v83, 2, v83
	ds_bpermute_b32 v83, v83, v75
	v_and_b32_e32 v0, 0xf0000000, v0
	v_or3_b32 v250, v81, v82, v0
	s_waitcnt lgkmcnt(0)
	v_add_u32_e32 v74, v75, v83
	v_cvt_f32_i32_e32 v74, v74
	v_mov_b32_e32 v0, 0
	v_mul_f32_e32 v251, 0.5, v74

.LBB0_1021:
	s_lshl_b32 s92, s21, 2
	s_cmp_lt_u32 s21, 0x80
	s_cselect_b32 s90, s86, s88
	s_cselect_b32 s91, s87, s89
	s_cselect_b32 s92, s92, 0
	s_add_u32 s90, s90, s92
	s_addc_u32 s91, s91, 0
	s_load_dwordx16 s[64:79], s[90:91], 0x40 glc
	v_perm_b32 v149, v186, v190, s29
	v_dot2c_f32_f16_e32 v224, s47, v149
	v_and_b32_e32 v149, s32, v149
	v_dot2c_f32_f16_e32 v220, s47, v149
	v_perm_b32 v149, v186, v190, s30
	v_dot2c_f32_f16_e32 v225, s47, v149
	v_and_b32_e32 v149, s32, v149
	v_dot2c_f32_f16_e32 v221, s47, v149
	v_perm_b32 v149, v186, v190, s31
	v_perm_b32 v117, v186, v190, s33
	v_dot2c_f32_f16_e32 v223, s47, v117
	v_and_b32_e32 v117, s32, v117
	v_dot2c_f32_f16_e32 v222, s47, v149
	v_and_b32_e32 v149, s32, v149
	v_dot2c_f32_f16_e32 v219, s47, v117
	v_dot2c_f32_f16_e32 v218, s47, v149
	v_perm_b32 v149, v187, v191, s29
	v_dot2c_f32_f16_e32 v216, s47, v149
	v_and_b32_e32 v149, s32, v149
	v_dot2c_f32_f16_e32 v212, s47, v149
	v_perm_b32 v149, v187, v191, s30
	v_dot2c_f32_f16_e32 v217, s47, v149
	v_and_b32_e32 v149, s32, v149
	v_dot2c_f32_f16_e32 v213, s47, v149
	v_perm_b32 v149, v187, v191, s31
	v_perm_b32 v117, v187, v191, s33
	v_dot2c_f32_f16_e32 v215, s47, v117
	v_and_b32_e32 v117, s32, v117
	v_dot2c_f32_f16_e32 v214, s47, v149
	v_and_b32_e32 v149, s32, v149
	v_dot2c_f32_f16_e32 v211, s47, v117
	v_dot2c_f32_f16_e32 v210, s47, v149
	v_perm_b32 v149, v178, v182, s29
	v_dot2c_f32_f16_e32 v224, s45, v149
	v_and_b32_e32 v149, s32, v149
	v_dot2c_f32_f16_e32 v220, s45, v149
	v_perm_b32 v149, v178, v182, s30
	v_dot2c_f32_f16_e32 v225, s45, v149
	v_and_b32_e32 v149, s32, v149
	v_dot2c_f32_f16_e32 v221, s45, v149
	v_perm_b32 v149, v178, v182, s31
	v_perm_b32 v117, v178, v182, s33
	v_dot2c_f32_f16_e32 v223, s45, v117
	v_and_b32_e32 v117, s32, v117
	v_dot2c_f32_f16_e32 v222, s45, v149
	v_and_b32_e32 v149, s32, v149
	v_dot2c_f32_f16_e32 v219, s45, v117
	v_dot2c_f32_f16_e32 v218, s45, v149
	v_perm_b32 v149, v179, v183, s29
	v_dot2c_f32_f16_e32 v216, s45, v149
	v_and_b32_e32 v149, s32, v149
	v_dot2c_f32_f16_e32 v212, s45, v149
	v_perm_b32 v149, v179, v183, s30
	v_dot2c_f32_f16_e32 v217, s45, v149
	v_and_b32_e32 v149, s32, v149
	v_dot2c_f32_f16_e32 v213, s45, v149
	v_perm_b32 v149, v179, v183, s31
	v_perm_b32 v117, v179, v183, s33
	v_dot2c_f32_f16_e32 v215, s45, v117
	v_and_b32_e32 v117, s32, v117
	v_dot2c_f32_f16_e32 v214, s45, v149
	v_and_b32_e32 v149, s32, v149
	v_dot2c_f32_f16_e32 v211, s45, v117
	v_dot2c_f32_f16_e32 v210, s45, v149
	v_perm_b32 v149, v170, v174, s29
	v_dot2c_f32_f16_e32 v224, s43, v149
	v_and_b32_e32 v149, s32, v149
	v_dot2c_f32_f16_e32 v220, s43, v149
	v_perm_b32 v149, v170, v174, s30
	v_dot2c_f32_f16_e32 v225, s43, v149
	v_and_b32_e32 v149, s32, v149
	v_dot2c_f32_f16_e32 v221, s43, v149
	v_perm_b32 v149, v170, v174, s31
	v_perm_b32 v117, v170, v174, s33
	v_dot2c_f32_f16_e32 v223, s43, v117
	v_and_b32_e32 v117, s32, v117
	v_dot2c_f32_f16_e32 v222, s43, v149
	v_and_b32_e32 v149, s32, v149
	v_dot2c_f32_f16_e32 v219, s43, v117
	v_dot2c_f32_f16_e32 v218, s43, v149
	v_perm_b32 v149, v171, v175, s29
	v_dot2c_f32_f16_e32 v216, s43, v149
	v_and_b32_e32 v149, s32, v149
	v_dot2c_f32_f16_e32 v212, s43, v149
	v_perm_b32 v149, v171, v175, s30
	v_dot2c_f32_f16_e32 v217, s43, v149
	v_and_b32_e32 v149, s32, v149
	v_dot2c_f32_f16_e32 v213, s43, v149
	v_perm_b32 v149, v171, v175, s31
	v_perm_b32 v117, v171, v175, s33
	v_dot2c_f32_f16_e32 v215, s43, v117
	v_and_b32_e32 v117, s32, v117
	v_dot2c_f32_f16_e32 v214, s43, v149
	v_and_b32_e32 v149, s32, v149
	v_dot2c_f32_f16_e32 v211, s43, v117
	v_dot2c_f32_f16_e32 v210, s43, v149
	v_perm_b32 v149, v162, v166, s29
	v_dot2c_f32_f16_e32 v224, s41, v149
	v_and_b32_e32 v149, s32, v149
	v_dot2c_f32_f16_e32 v220, s41, v149
	v_perm_b32 v149, v162, v166, s30
	v_dot2c_f32_f16_e32 v225, s41, v149
	v_and_b32_e32 v149, s32, v149
	v_dot2c_f32_f16_e32 v221, s41, v149
	v_perm_b32 v149, v162, v166, s31
	v_perm_b32 v117, v162, v166, s33
	v_dot2c_f32_f16_e32 v223, s41, v117
	v_and_b32_e32 v117, s32, v117
	v_dot2c_f32_f16_e32 v222, s41, v149
	v_and_b32_e32 v149, s32, v149
	v_dot2c_f32_f16_e32 v219, s41, v117
	v_dot2c_f32_f16_e32 v218, s41, v149
	v_perm_b32 v149, v163, v167, s29
	v_dot2c_f32_f16_e32 v216, s41, v149
	v_and_b32_e32 v149, s32, v149
	v_dot2c_f32_f16_e32 v212, s41, v149
	v_perm_b32 v149, v163, v167, s30
	v_dot2c_f32_f16_e32 v217, s41, v149
	v_and_b32_e32 v149, s32, v149
	v_dot2c_f32_f16_e32 v213, s41, v149
	v_perm_b32 v149, v163, v167, s31
	v_perm_b32 v117, v163, v167, s33
	v_dot2c_f32_f16_e32 v215, s41, v117
	v_and_b32_e32 v117, s32, v117
	v_dot2c_f32_f16_e32 v214, s41, v149
	v_and_b32_e32 v149, s32, v149
	v_dot2c_f32_f16_e32 v211, s41, v117
	v_dot2c_f32_f16_e32 v210, s41, v149
	v_perm_b32 v149, v154, v158, s29
	v_dot2c_f32_f16_e32 v224, s39, v149
	v_and_b32_e32 v149, s32, v149
	v_dot2c_f32_f16_e32 v220, s39, v149
	v_perm_b32 v149, v154, v158, s30
	v_dot2c_f32_f16_e32 v225, s39, v149
	v_and_b32_e32 v149, s32, v149
	v_dot2c_f32_f16_e32 v221, s39, v149
	v_perm_b32 v149, v154, v158, s31
	v_perm_b32 v117, v154, v158, s33
	v_dot2c_f32_f16_e32 v223, s39, v117
	v_and_b32_e32 v117, s32, v117
	v_dot2c_f32_f16_e32 v222, s39, v149
	v_and_b32_e32 v149, s32, v149
	v_dot2c_f32_f16_e32 v219, s39, v117
	v_dot2c_f32_f16_e32 v218, s39, v149
	v_perm_b32 v149, v155, v159, s29
	v_dot2c_f32_f16_e32 v216, s39, v149
	v_and_b32_e32 v149, s32, v149
	v_dot2c_f32_f16_e32 v212, s39, v149
	v_perm_b32 v149, v155, v159, s30
	v_dot2c_f32_f16_e32 v217, s39, v149
	v_and_b32_e32 v149, s32, v149
	v_dot2c_f32_f16_e32 v213, s39, v149
	v_perm_b32 v149, v155, v159, s31
	v_perm_b32 v117, v155, v159, s33
	v_dot2c_f32_f16_e32 v215, s39, v117
	v_and_b32_e32 v117, s32, v117
	v_dot2c_f32_f16_e32 v214, s39, v149
	v_and_b32_e32 v149, s32, v149
	v_dot2c_f32_f16_e32 v211, s39, v117
	v_perm_b32 v148, v146, v150, s29
	v_dot2c_f32_f16_e32 v224, s37, v148
	v_and_b32_e32 v148, s32, v148
	v_dot2c_f32_f16_e32 v220, s37, v148
	v_perm_b32 v148, v146, v150, s30
	v_dot2c_f32_f16_e32 v225, s37, v148
	v_and_b32_e32 v148, s32, v148
	v_dot2c_f32_f16_e32 v221, s37, v148
	v_perm_b32 v148, v146, v150, s31
	v_perm_b32 v117, v146, v150, s33
	v_dot2c_f32_f16_e32 v223, s37, v117
	v_and_b32_e32 v117, s32, v117
	v_dot2c_f32_f16_e32 v222, s37, v148
	v_and_b32_e32 v148, s32, v148
	v_dot2c_f32_f16_e32 v219, s37, v117
	v_perm_b32 v207, v147, v151, s29
	v_dot2c_f32_f16_e32 v216, s37, v207
	v_and_b32_e32 v207, s32, v207
	v_dot2c_f32_f16_e32 v212, s37, v207
	v_perm_b32 v207, v147, v151, s30
	v_dot2c_f32_f16_e32 v217, s37, v207
	v_and_b32_e32 v207, s32, v207
	v_dot2c_f32_f16_e32 v213, s37, v207
	v_perm_b32 v207, v147, v151, s31
	v_perm_b32 v117, v147, v151, s33
	v_dot2c_f32_f16_e32 v215, s37, v117
	v_and_b32_e32 v117, s32, v117
	v_dot2c_f32_f16_e32 v214, s37, v207
	v_and_b32_e32 v207, s32, v207
	v_dot2c_f32_f16_e32 v211, s37, v117
	v_perm_b32 v145, v114, v118, s29
	v_dot2c_f32_f16_e32 v224, s35, v145
	v_and_b32_e32 v145, s32, v145
	v_dot2c_f32_f16_e32 v220, s35, v145
	v_perm_b32 v145, v114, v118, s30
	v_dot2c_f32_f16_e32 v225, s35, v145
	v_and_b32_e32 v145, s32, v145
	v_dot2c_f32_f16_e32 v221, s35, v145
	v_perm_b32 v145, v114, v118, s31
	v_dot2c_f32_f16_e32 v222, s35, v145
	v_and_b32_e32 v145, s32, v145
	v_perm_b32 v117, v114, v118, s33
	v_and_b32_e32 v209, s32, v117
	v_dot2c_f32_f16_e32 v223, s35, v117
	v_dot2c_f32_f16_e32 v219, s35, v209
	v_perm_b32 v253, v115, v119, s29
	v_dot2c_f32_f16_e32 v216, s35, v253
	v_and_b32_e32 v253, s32, v253
	v_dot2c_f32_f16_e32 v212, s35, v253
	v_perm_b32 v253, v115, v119, s30
	v_dot2c_f32_f16_e32 v217, s35, v253
	v_and_b32_e32 v253, s32, v253
	v_dot2c_f32_f16_e32 v213, s35, v253
	v_perm_b32 v253, v115, v119, s31
	v_perm_b32 v209, v115, v119, s33
	v_dot2c_f32_f16_e32 v215, s35, v209
	v_and_b32_e32 v209, s32, v209
	v_dot2c_f32_f16_e32 v214, s35, v253
	v_and_b32_e32 v253, s32, v253
	v_dot2c_f32_f16_e32 v211, s35, v209
	v_perm_b32 v117, v68, v72, s29
	v_dot2c_f32_f16_e32 v224, s4, v117
	v_and_b32_e32 v117, s32, v117
	v_dot2c_f32_f16_e32 v220, s4, v117
	v_perm_b32 v117, v68, v72, s30
	v_dot2c_f32_f16_e32 v225, s4, v117
	v_and_b32_e32 v117, s32, v117
	v_dot2c_f32_f16_e32 v221, s4, v117
	v_perm_b32 v117, v68, v72, s31
	v_dot2c_f32_f16_e32 v222, s4, v117
	v_and_b32_e32 v117, s32, v117
	v_perm_b32 v254, v68, v72, s33
	v_and_b32_e32 v254, s32, v254
	v_perm_b32 v209, v68, v72, s33
	v_dot2c_f32_f16_e32 v219, s4, v254
	v_dot2c_f32_f16_e32 v223, s4, v209
	v_perm_b32 v209, v69, v73, s29
	v_dot2c_f32_f16_e32 v216, s4, v209
	v_and_b32_e32 v209, s32, v209
	v_dot2c_f32_f16_e32 v212, s4, v209
	v_perm_b32 v209, v69, v73, s30
	v_dot2c_f32_f16_e32 v217, s4, v209
	v_and_b32_e32 v209, s32, v209
	v_dot2c_f32_f16_e32 v213, s4, v209
	v_perm_b32 v209, v69, v73, s31
	v_perm_b32 v254, v69, v73, s33
	v_dot2c_f32_f16_e32 v215, s4, v254
	s_waitcnt vmcnt(31)
	v_dot8_i32_i4 v68, v248, v62, 0
	v_dot8_i32_i4 v68, v250, v63, v68
	v_dot2c_f32_f16_e32 v210, s39, v149
	v_dot2c_f32_f16_e32 v218, s37, v148
	v_dot2c_f32_f16_e32 v210, s37, v207
	v_lshlrev_b32_e32 v68, 4, v68
	v_dot8_i32_i4 v68, v247, v62, v68
	s_waitcnt vmcnt(30)
	v_dot8_i32_i4 v62, v248, v58, 0
	v_dot8_i32_i4 v62, v250, v59, v62
	v_dot8_i32_i4 v68, v249, v63, v68
	v_dot2c_f32_f16_e32 v218, s35, v145
	v_dot2c_f32_f16_e32 v210, s35, v253
	v_lshlrev_b32_e32 v62, 4, v62
	v_dot8_i32_i4 v62, v247, v58, v62
	s_waitcnt vmcnt(29)
	v_dot8_i32_i4 v58, v248, v54, 0
	v_dot8_i32_i4 v58, v250, v55, v58
	v_dot8_i32_i4 v62, v249, v59, v62
	v_dot2c_f32_f16_e32 v214, s4, v209
	v_and_b32_e32 v209, s32, v209
	v_lshlrev_b32_e32 v58, 4, v58
	v_dot8_i32_i4 v58, v247, v54, v58
	s_waitcnt vmcnt(28)
	v_dot8_i32_i4 v54, v248, v50, 0
	v_dot8_i32_i4 v54, v250, v51, v54
	v_dot8_i32_i4 v58, v249, v55, v58
	v_dot2c_f32_f16_e32 v218, s4, v117
	v_dot2c_f32_f16_e32 v210, s4, v209
	v_lshlrev_b32_e32 v54, 4, v54
	v_dot8_i32_i4 v54, v247, v50, v54
	s_waitcnt vmcnt(27)
	v_dot8_i32_i4 v50, v248, v46, 0
	v_dot8_i32_i4 v50, v250, v47, v50
	v_dot8_i32_i4 v54, v249, v51, v54
	s_add_i32 s24, s25, 2
	s_cmp_lt_u32 s25, 5
	v_lshlrev_b32_e32 v50, 4, v50
	v_dot8_i32_i4 v50, v247, v46, v50
	s_waitcnt vmcnt(26)
	v_dot8_i32_i4 v46, v248, v42, 0
	v_dot8_i32_i4 v46, v250, v43, v46
	v_dot8_i32_i4 v50, v249, v47, v50
	v_cvt_f32_f16_e32 v116, v116
	s_nop 0
	v_lshlrev_b32_e32 v46, 4, v46
	v_dot8_i32_i4 v46, v247, v42, v46
	s_waitcnt vmcnt(25)
	v_dot8_i32_i4 v42, v248, v38, 0
	v_dot8_i32_i4 v42, v250, v39, v42
	v_dot8_i32_i4 v46, v249, v43, v46
	s_nop 1
	v_lshlrev_b32_e32 v42, 4, v42
	v_dot8_i32_i4 v42, v247, v38, v42
	s_waitcnt vmcnt(24)
	v_dot8_i32_i4 v38, v248, v30, 0
	v_dot8_i32_i4 v38, v250, v31, v38
	v_dot8_i32_i4 v42, v249, v39, v42
	s_nop 1
	v_lshlrev_b32_e32 v38, 4, v38
	v_dot8_i32_i4 v38, v247, v30, v38
	v_dot8_i32_i4 v38, v249, v31, v38
	s_waitcnt vmcnt(22)
	v_dot8_i32_i4 v31, v248, v22, 0
	v_dot8_i32_i4 v31, v250, v23, v31
	v_dot8_i32_i4 v30, v248, v34, 0
	v_dot8_i32_i4 v30, v250, v35, v30
	s_nop 0
	v_lshlrev_b32_e32 v31, 4, v31
	v_dot8_i32_i4 v31, v247, v22, v31
	v_dot8_i32_i4 v31, v249, v23, v31
	s_waitcnt vmcnt(20)
	v_dot8_i32_i4 v23, v248, v14, 0
	v_dot8_i32_i4 v23, v250, v15, v23
	v_dot8_i32_i4 v22, v248, v26, 0
	v_dot8_i32_i4 v22, v250, v27, v22
	s_nop 0
	v_lshlrev_b32_e32 v23, 4, v23
	v_dot8_i32_i4 v23, v247, v14, v23
	v_dot8_i32_i4 v23, v249, v15, v23
	s_waitcnt vmcnt(18)
	v_dot8_i32_i4 v15, v248, v6, 0
	v_dot8_i32_i4 v15, v250, v7, v15
	v_dot8_i32_i4 v14, v248, v18, 0
	v_dot8_i32_i4 v14, v250, v19, v14
	s_nop 0
	v_lshlrev_b32_e32 v15, 4, v15
	v_dot8_i32_i4 v15, v247, v6, v15
	v_dot8_i32_i4 v15, v249, v7, v15
	s_waitcnt vmcnt(17)
	v_dot8_i32_i4 v6, v248, v10, 0
	s_waitcnt vmcnt(16)
	v_dot8_i32_i4 v7, v248, v2, 0
	v_dot8_i32_i4 v6, v250, v11, v6
	v_dot8_i32_i4 v7, v250, v3, v7
	v_lshlrev_b32_e32 v30, 4, v30
	v_lshlrev_b32_e32 v22, 4, v22
	v_lshlrev_b32_e32 v14, 4, v14
	v_lshlrev_b32_e32 v6, 4, v6
	v_lshlrev_b32_e32 v7, 4, v7
	v_dot8_i32_i4 v30, v247, v34, v30
	v_dot8_i32_i4 v22, v247, v26, v22
	v_dot8_i32_i4 v14, v247, v18, v14
	v_dot8_i32_i4 v6, v247, v10, v6
	v_dot8_i32_i4 v7, v247, v2, v7
	v_dot8_i32_i4 v30, v249, v35, v30
	v_dot8_i32_i4 v22, v249, v27, v22
	v_dot8_i32_i4 v14, v249, v19, v14
	v_dot8_i32_i4 v6, v249, v11, v6
	v_dot8_i32_i4 v7, v249, v3, v7
	v_permlane32_swap_b32_e32 v68, v30
	v_permlane32_swap_b32_e32 v62, v31
	v_permlane32_swap_b32_e32 v58, v22
	v_permlane32_swap_b32_e32 v54, v23
	v_permlane32_swap_b32_e32 v50, v14
	v_permlane32_swap_b32_e32 v46, v15
	v_permlane32_swap_b32_e32 v42, v6
	v_permlane32_swap_b32_e32 v38, v7
	v_add_u32_e32 v2, v68, v30
	v_add_u32_e32 v3, v62, v31
	v_add_u32_e32 v10, v58, v22
	v_add_u32_e32 v11, v54, v23
	v_add_u32_e32 v14, v50, v14
	v_add_u32_e32 v15, v46, v15
	v_add_u32_e32 v6, v42, v6
	v_add_u32_e32 v7, v38, v7
	v_permlane16_swap_b32_e32 v2, v14
	v_permlane16_swap_b32_e32 v3, v15
	v_permlane16_swap_b32_e32 v10, v6
	v_permlane16_swap_b32_e32 v11, v7
	v_add_u32_e32 v2, v2, v14
	v_add_u32_e32 v3, v3, v15
	v_add_u32_e32 v6, v10, v6
	v_add_u32_e32 v7, v11, v7
	v_cndmask_b32_e64 v10, v6, v2, s[0:1]
	v_cndmask_b32_e64 v2, v2, v6, s[0:1]
	v_cndmask_b32_e64 v6, v7, v3, s[0:1]
	v_cndmask_b32_e64 v3, v3, v7, s[0:1]
	v_add_u32_dpp v2, v2, v10 quad_perm:[2,3,0,1] row_mask:0xf bank_mask:0xf bound_ctrl:1
	s_waitcnt lgkmcnt(0)
	ds_bpermute_b32 v7, v66, v71 offset:64
	v_add_u32_dpp v3, v3, v6 quad_perm:[2,3,0,1] row_mask:0xf bank_mask:0xf bound_ctrl:1
	v_cndmask_b32_e64 v6, v3, v2, s[2:3]
	v_cndmask_b32_e64 v2, v2, v3, s[2:3]
	ds_bpermute_b32 v3, v66, v70 offset:64
	v_add_f32_e32 v68, v252, v116
	v_add_u32_dpp v2, v2, v6 quad_perm:[1,0,3,2] row_mask:0xf bank_mask:0xf bound_ctrl:1
	v_and_b32_e32 v6, s32, v254
	v_dot2c_f32_f16_e32 v211, s4, v6
	v_add_u32_dpp v2, v2, v2 row_ror:8 row_mask:0xf bank_mask:0xf bound_ctrl:1
	ds_bpermute_b32 v6, v66, v67 offset:64
	s_nop 0
	v_add_u32_dpp v2, v2, v2 row_ror:4 row_mask:0xf bank_mask:0xf bound_ctrl:1
	v_cvt_f32_i32_e32 v2, v2
	v_add_f32_e32 v2, v251, v2
	v_mul_f32_e32 v2, v244, v2
	s_waitcnt lgkmcnt(1)
	v_mul_f32_e32 v2, v2, v3
	v_fma_f32 v3, |v2|, s28, 1.0
	v_rcp_f32_e32 v3, v3
	v_mul_f32_e32 v11, v2, v2
	v_mul_f32_e32 v11, 0xbf38aa3b, v11
	v_exp_f32_e32 v11, v11
	v_fmamk_f32 v10, v3, 0x3f07dc22, v227
	v_fmaak_f32 v10, v3, v10, 0x3f35f0e3
	v_fmaak_f32 v10, v3, v10, 0xbe11a98e
	v_fmaak_f32 v10, v3, v10, 0x3e027906
	v_mul_f32_e32 v3, v3, v10
	v_mul_f32_e32 v3, v11, v3
	v_mul_f32_e32 v10, v2, v3
	v_fma_f32 v3, -v2, v3, v2
	v_cmp_gt_f32_e64 s[4:5], 0, v2
	s_nop 1
	v_cndmask_b32_e64 v2, v3, v10, s[4:5]
	s_waitcnt lgkmcnt(0)
	v_mul_f32_e32 v2, v2, v6
	v_mul_f32_e32 v2, v2, v7
	v_fma_mixlo_f16 v2, v2, s16, 0
	v_and_b32_e32 v3, 0xffff, v2
	s_cselect_b64 s[4:5], -1, 0
	s_nop 0
	v_mov_b32_dpp v253, v3 quad_perm:[1,0,3,2] row_mask:0xf bank_mask:0xf
	v_lshl_or_b32 v254, v253, 16, v3
	v_cvt_f32_f16_e32 v66, v2
	v_readlane_b32 s5, v254, 0
	v_perm_b32 v14, v60, v64, s29
	s_nop 0
	v_dot2c_f32_f16_e32 v224, s5, v14
	v_and_b32_e32 v14, s32, v14
	v_dot2c_f32_f16_e32 v220, s5, v14
	v_perm_b32 v14, v60, v64, s30
	v_dot2c_f32_f16_e32 v225, s5, v14
	v_and_b32_e32 v14, s32, v14
	v_dot2c_f32_f16_e32 v221, s5, v14
	v_perm_b32 v14, v60, v64, s31
	v_perm_b32 v6, v60, v64, s33
	v_dot2c_f32_f16_e32 v223, s5, v6
	v_and_b32_e32 v6, s32, v6
	v_dot2c_f32_f16_e32 v222, s5, v14
	v_and_b32_e32 v14, s32, v14
	v_dot2c_f32_f16_e32 v219, s5, v6
	v_dot2c_f32_f16_e32 v218, s5, v14
	v_perm_b32 v14, v61, v65, s29
	v_dot2c_f32_f16_e32 v216, s5, v14
	v_and_b32_e32 v14, s32, v14
	v_dot2c_f32_f16_e32 v212, s5, v14
	v_perm_b32 v14, v61, v65, s30
	v_dot2c_f32_f16_e32 v217, s5, v14
	v_and_b32_e32 v14, s32, v14
	v_dot2c_f32_f16_e32 v213, s5, v14
	v_perm_b32 v14, v61, v65, s31
	v_perm_b32 v6, v61, v65, s33
	v_dot2c_f32_f16_e32 v214, s5, v14
	v_and_b32_e32 v14, s32, v14
	v_dot2c_f32_f16_e32 v215, s5, v6
	v_and_b32_e32 v6, s32, v6
	v_dot2c_f32_f16_e32 v210, s5, v14
	v_dot2c_f32_f16_e32 v211, s5, v6
	v_readlane_b32 s4, v254, 2
	buffer_load_dwordx4 v[62:65], v194, s[80:83], s64 offen
	buffer_load_dwordx4 v[58:61], v194, s[80:83], s65 offen
	v_perm_b32 v14, v52, v56, s29
	v_dot2c_f32_f16_e32 v224, s4, v14
	v_and_b32_e32 v14, s32, v14
	v_dot2c_f32_f16_e32 v220, s4, v14
	v_perm_b32 v14, v52, v56, s30
	v_dot2c_f32_f16_e32 v225, s4, v14
	v_and_b32_e32 v14, s32, v14
	v_dot2c_f32_f16_e32 v221, s4, v14
	v_perm_b32 v14, v52, v56, s31
	v_perm_b32 v6, v52, v56, s33
	v_dot2c_f32_f16_e32 v223, s4, v6
	v_and_b32_e32 v6, s32, v6
	v_dot2c_f32_f16_e32 v222, s4, v14
	v_and_b32_e32 v14, s32, v14
	v_dot2c_f32_f16_e32 v219, s4, v6
	v_dot2c_f32_f16_e32 v218, s4, v14
	v_perm_b32 v14, v53, v57, s29
	v_dot2c_f32_f16_e32 v216, s4, v14
	v_and_b32_e32 v14, s32, v14
	v_dot2c_f32_f16_e32 v212, s4, v14
	v_perm_b32 v14, v53, v57, s30
	v_dot2c_f32_f16_e32 v217, s4, v14
	v_and_b32_e32 v14, s32, v14
	v_dot2c_f32_f16_e32 v213, s4, v14
	v_perm_b32 v14, v53, v57, s31
	v_perm_b32 v6, v53, v57, s33
	v_dot2c_f32_f16_e32 v214, s4, v14
	v_and_b32_e32 v14, s32, v14
	v_dot2c_f32_f16_e32 v215, s4, v6
	v_and_b32_e32 v6, s32, v6
	v_dot2c_f32_f16_e32 v210, s4, v14
	v_dot2c_f32_f16_e32 v211, s4, v6
	v_readlane_b32 s4, v254, 16
	buffer_load_dwordx4 v[54:57], v194, s[80:83], s66 offen
	buffer_load_dwordx4 v[50:53], v194, s[80:83], s67 offen
	v_perm_b32 v14, v44, v48, s29
	v_dot2c_f32_f16_e32 v224, s4, v14
	v_and_b32_e32 v14, s32, v14
	v_dot2c_f32_f16_e32 v220, s4, v14
	v_perm_b32 v14, v44, v48, s30
	v_dot2c_f32_f16_e32 v225, s4, v14
	v_and_b32_e32 v14, s32, v14
	v_dot2c_f32_f16_e32 v221, s4, v14
	v_perm_b32 v14, v44, v48, s31
	v_perm_b32 v6, v44, v48, s33
	v_dot2c_f32_f16_e32 v223, s4, v6
	v_and_b32_e32 v6, s32, v6
	v_dot2c_f32_f16_e32 v222, s4, v14
	v_and_b32_e32 v14, s32, v14
	v_dot2c_f32_f16_e32 v219, s4, v6
	v_dot2c_f32_f16_e32 v218, s4, v14
	v_perm_b32 v14, v45, v49, s29
	v_dot2c_f32_f16_e32 v216, s4, v14
	v_and_b32_e32 v14, s32, v14
	v_dot2c_f32_f16_e32 v212, s4, v14
	v_perm_b32 v14, v45, v49, s30
	v_dot2c_f32_f16_e32 v217, s4, v14
	v_and_b32_e32 v14, s32, v14
	v_dot2c_f32_f16_e32 v213, s4, v14
	v_perm_b32 v14, v45, v49, s31
	v_perm_b32 v6, v45, v49, s33
	v_dot2c_f32_f16_e32 v214, s4, v14
	v_and_b32_e32 v14, s32, v14
	v_dot2c_f32_f16_e32 v215, s4, v6
	v_and_b32_e32 v6, s32, v6
	v_dot2c_f32_f16_e32 v210, s4, v14
	v_dot2c_f32_f16_e32 v211, s4, v6
	v_readlane_b32 s4, v254, 18
	buffer_load_dwordx4 v[46:49], v194, s[80:83], s68 offen
	buffer_load_dwordx4 v[42:45], v194, s[80:83], s69 offen
	v_perm_b32 v14, v32, v40, s29
	v_dot2c_f32_f16_e32 v224, s4, v14
	v_and_b32_e32 v14, s32, v14
	v_dot2c_f32_f16_e32 v220, s4, v14
	v_perm_b32 v14, v32, v40, s30
	v_dot2c_f32_f16_e32 v225, s4, v14
	v_and_b32_e32 v14, s32, v14
	v_dot2c_f32_f16_e32 v221, s4, v14
	v_perm_b32 v14, v32, v40, s31
	v_perm_b32 v6, v32, v40, s33
	v_dot2c_f32_f16_e32 v223, s4, v6
	v_and_b32_e32 v6, s32, v6
	v_dot2c_f32_f16_e32 v222, s4, v14
	v_and_b32_e32 v14, s32, v14
	v_dot2c_f32_f16_e32 v219, s4, v6
	v_dot2c_f32_f16_e32 v218, s4, v14
	v_perm_b32 v14, v33, v41, s29
	v_dot2c_f32_f16_e32 v216, s4, v14
	v_and_b32_e32 v14, s32, v14
	v_dot2c_f32_f16_e32 v212, s4, v14
	v_perm_b32 v14, v33, v41, s30
	v_dot2c_f32_f16_e32 v217, s4, v14
	v_and_b32_e32 v14, s32, v14
	v_dot2c_f32_f16_e32 v213, s4, v14
	v_perm_b32 v14, v33, v41, s31
	v_perm_b32 v6, v33, v41, s33
	v_dot2c_f32_f16_e32 v214, s4, v14
	v_and_b32_e32 v14, s32, v14
	v_dot2c_f32_f16_e32 v215, s4, v6
	v_and_b32_e32 v6, s32, v6
	v_dot2c_f32_f16_e32 v210, s4, v14
	v_dot2c_f32_f16_e32 v211, s4, v6
	v_readlane_b32 s4, v254, 32
	buffer_load_dwordx4 v[38:41], v194, s[80:83], s70 offen
	buffer_load_dwordx4 v[30:33], v194, s[80:83], s71 offen
	v_perm_b32 v14, v24, v36, s29
	v_dot2c_f32_f16_e32 v224, s4, v14
	v_and_b32_e32 v14, s32, v14
	v_dot2c_f32_f16_e32 v220, s4, v14
	v_perm_b32 v14, v24, v36, s30
	v_dot2c_f32_f16_e32 v225, s4, v14
	v_and_b32_e32 v14, s32, v14
	v_dot2c_f32_f16_e32 v221, s4, v14
	v_perm_b32 v14, v24, v36, s31
	v_perm_b32 v6, v24, v36, s33
	v_dot2c_f32_f16_e32 v223, s4, v6
	v_and_b32_e32 v6, s32, v6
	v_dot2c_f32_f16_e32 v222, s4, v14
	v_and_b32_e32 v14, s32, v14
	v_dot2c_f32_f16_e32 v219, s4, v6
	v_dot2c_f32_f16_e32 v218, s4, v14
	v_perm_b32 v14, v25, v37, s29
	v_dot2c_f32_f16_e32 v216, s4, v14
	v_and_b32_e32 v14, s32, v14
	v_dot2c_f32_f16_e32 v212, s4, v14
	v_perm_b32 v14, v25, v37, s30
	v_dot2c_f32_f16_e32 v217, s4, v14
	v_and_b32_e32 v14, s32, v14
	v_dot2c_f32_f16_e32 v213, s4, v14
	v_perm_b32 v14, v25, v37, s31
	v_perm_b32 v6, v25, v37, s33
	v_dot2c_f32_f16_e32 v214, s4, v14
	v_and_b32_e32 v14, s32, v14
	v_dot2c_f32_f16_e32 v215, s4, v6
	v_and_b32_e32 v6, s32, v6
	v_dot2c_f32_f16_e32 v210, s4, v14
	v_dot2c_f32_f16_e32 v211, s4, v6
	v_readlane_b32 s4, v254, 34
	buffer_load_dwordx4 v[34:37], v194, s[80:83], s72 offen
	buffer_load_dwordx4 v[22:25], v194, s[80:83], s73 offen
	v_perm_b32 v14, v16, v28, s29
	v_dot2c_f32_f16_e32 v224, s4, v14
	v_and_b32_e32 v14, s32, v14
	v_dot2c_f32_f16_e32 v220, s4, v14
	v_perm_b32 v14, v16, v28, s30
	v_dot2c_f32_f16_e32 v225, s4, v14
	v_and_b32_e32 v14, s32, v14
	v_dot2c_f32_f16_e32 v221, s4, v14
	v_perm_b32 v14, v16, v28, s31
	v_perm_b32 v6, v16, v28, s33
	v_dot2c_f32_f16_e32 v223, s4, v6
	v_and_b32_e32 v6, s32, v6
	v_dot2c_f32_f16_e32 v222, s4, v14
	v_and_b32_e32 v14, s32, v14
	v_dot2c_f32_f16_e32 v219, s4, v6
	v_dot2c_f32_f16_e32 v218, s4, v14
	v_perm_b32 v14, v17, v29, s29
; __device__ __forceinline__ void expert_tokens(const unsigned char* __restrict__ UV, const float* __restrict__ US, const float* __restrict__ VS, ...
;     ...
;         for (int bi = 0; bi < 128 / EB; bi += 2) {
;             EXP_STEP(A, bi);
;             if (bi == 0) { nsu0 = US[ni0]; nsu1 = US[ni1]; nsv0 = VS[ni0]; nsv1 = VS[ni1]; }
;             EXP_STEP(B, bi + 1);
;         }
	v_dot2c_f32_f16_e32 v216, s4, v14
	v_and_b32_e32 v14, s32, v14
	v_dot2c_f32_f16_e32 v212, s4, v14
	v_perm_b32 v14, v17, v29, s30
	v_dot2c_f32_f16_e32 v217, s4, v14
	v_and_b32_e32 v14, s32, v14
	v_dot2c_f32_f16_e32 v213, s4, v14
	v_perm_b32 v14, v17, v29, s31
	v_perm_b32 v6, v17, v29, s33
	v_dot2c_f32_f16_e32 v214, s4, v14
	v_and_b32_e32 v14, s32, v14
	v_dot2c_f32_f16_e32 v215, s4, v6
	v_and_b32_e32 v6, s32, v6
	v_dot2c_f32_f16_e32 v210, s4, v14
	v_dot2c_f32_f16_e32 v211, s4, v6
	v_readlane_b32 s4, v254, 48
	buffer_load_dwordx4 v[26:29], v194, s[80:83], s74 offen
	buffer_load_dwordx4 v[14:17], v194, s[80:83], s75 offen
	v_perm_b32 v11, v8, v20, s29
	v_dot2c_f32_f16_e32 v224, s4, v11
	v_and_b32_e32 v11, s32, v11
	v_dot2c_f32_f16_e32 v220, s4, v11
	v_perm_b32 v11, v8, v20, s30
	v_dot2c_f32_f16_e32 v225, s4, v11
	v_and_b32_e32 v11, s32, v11
	v_dot2c_f32_f16_e32 v221, s4, v11
	v_perm_b32 v11, v8, v20, s31
	v_perm_b32 v6, v8, v20, s33
	v_dot2c_f32_f16_e32 v223, s4, v6
	v_and_b32_e32 v6, s32, v6
	v_dot2c_f32_f16_e32 v222, s4, v11
	v_and_b32_e32 v11, s32, v11
	v_dot2c_f32_f16_e32 v219, s4, v6
	v_perm_b32 v10, v9, v21, s29
	v_dot2c_f32_f16_e32 v216, s4, v10
	v_and_b32_e32 v10, s32, v10
	v_dot2c_f32_f16_e32 v212, s4, v10
	v_perm_b32 v10, v9, v21, s30
	v_dot2c_f32_f16_e32 v217, s4, v10
	v_and_b32_e32 v10, s32, v10
	v_dot2c_f32_f16_e32 v213, s4, v10
	v_perm_b32 v10, v9, v21, s31
	v_perm_b32 v6, v9, v21, s33
	v_dot2c_f32_f16_e32 v214, s4, v10
	v_and_b32_e32 v10, s32, v10
	v_dot2c_f32_f16_e32 v215, s4, v6
	v_and_b32_e32 v6, s32, v6
	v_dot2c_f32_f16_e32 v218, s4, v11
	v_dot2c_f32_f16_e32 v210, s4, v10
	v_dot2c_f32_f16_e32 v211, s4, v6
	v_readlane_b32 s4, v254, 50
	buffer_load_dwordx4 v[18:21], v194, s[80:83], s76 offen
	buffer_load_dwordx4 v[6:9], v194, s[80:83], s77 offen
	v_perm_b32 v254, v4, v12, s29
	v_dot2c_f32_f16_e32 v224, s4, v254
	v_and_b32_e32 v254, s32, v254
	v_dot2c_f32_f16_e32 v220, s4, v254
	v_perm_b32 v254, v4, v12, s30
	v_dot2c_f32_f16_e32 v225, s4, v254
	v_and_b32_e32 v254, s32, v254
	v_dot2c_f32_f16_e32 v221, s4, v254
	v_perm_b32 v254, v4, v12, s31
	v_perm_b32 v3, v4, v12, s33
	v_dot2c_f32_f16_e32 v223, s4, v3
	v_and_b32_e32 v3, s32, v3
	v_dot2c_f32_f16_e32 v222, s4, v254
	v_and_b32_e32 v254, s32, v254
	v_dot2c_f32_f16_e32 v219, s4, v3
	v_perm_b32 v11, v5, v13, s29
	v_dot2c_f32_f16_e32 v216, s4, v11
	v_and_b32_e32 v11, s32, v11
	v_dot2c_f32_f16_e32 v212, s4, v11
	v_perm_b32 v11, v5, v13, s30
	v_dot2c_f32_f16_e32 v217, s4, v11
	v_and_b32_e32 v11, s32, v11
	v_dot2c_f32_f16_e32 v213, s4, v11
	v_perm_b32 v11, v5, v13, s31
	v_perm_b32 v3, v5, v13, s33
	v_dot2c_f32_f16_e32 v214, s4, v11
	v_and_b32_e32 v11, s32, v11
	v_dot2c_f32_f16_e32 v215, s4, v3
	v_and_b32_e32 v3, s32, v3
	v_dot2c_f32_f16_e32 v218, s4, v254
	v_dot2c_f32_f16_e32 v210, s4, v11
	v_dot2c_f32_f16_e32 v211, s4, v3
	buffer_load_dwordx4 v[10:13], v194, s[80:83], s78 offen
	buffer_load_dwordx4 v[2:5], v194, s[80:83], s79 offen
	v_add_f32_e32 v252, v68, v66
	s_add_i32 s21, s21, 32
	s_and_b64 vcc, exec, s[22:23]
	s_cbranch_vccnz .LBB0_1013
	s_waitcnt vmcnt(16)
	v_mov_b64_e32 v[158:159], v[112:113]
	v_mov_b64_e32 v[190:191], v[80:81]
	v_mov_b64_e32 v[186:187], v[76:77]
	v_mov_b64_e32 v[182:183], v[88:89]
	v_mov_b64_e32 v[178:179], v[84:85]
	v_mov_b64_e32 v[174:175], v[96:97]
	v_mov_b64_e32 v[170:171], v[92:93]
	v_mov_b64_e32 v[166:167], v[104:105]
	v_mov_b64_e32 v[162:163], v[100:101]
	v_mov_b64_e32 v[156:157], v[110:111]
	v_mov_b64_e32 v[154:155], v[108:109]
	v_mov_b64_e32 v[150:151], v[126:127]
	v_mov_b64_e32 v[146:147], v[122:123]
	v_mov_b64_e32 v[116:117], v[132:133]
	v_mov_b64_e32 v[112:113], v[128:129]
	v_mov_b64_e32 v[70:71], v[140:141]
	v_mov_b64_e32 v[66:67], v[136:137]
	v_mov_b64_e32 v[188:189], v[78:79]
	v_mov_b64_e32 v[184:185], v[74:75]
	v_mov_b64_e32 v[180:181], v[86:87]
	v_mov_b64_e32 v[176:177], v[82:83]
	v_mov_b64_e32 v[172:173], v[94:95]
	v_mov_b64_e32 v[168:169], v[90:91]
	v_mov_b64_e32 v[164:165], v[102:103]
	v_mov_b64_e32 v[160:161], v[98:99]
	v_mov_b64_e32 v[152:153], v[106:107]
	v_mov_b64_e32 v[148:149], v[124:125]
	v_mov_b64_e32 v[144:145], v[120:121]
	v_mov_b64_e32 v[118:119], v[134:135]
	v_mov_b64_e32 v[114:115], v[130:131]
	v_mov_b64_e32 v[72:73], v[142:143]
	v_mov_b64_e32 v[68:69], v[138:139]
	s_mov_b32 s25, s24
	s_branch .LBB0_1019
